# MoBA phase A: q-row and kmax loads issued at the top of the pass (overlap the block-mean staging round trip and its barriers)
# baseline (speedup 1.0000x reference)
; #define LAS __attribute__((address_space(3)))
; __global__ void __launch_bounds__(NWAVES * 64, 2) mk_fwd(Args args) {
;     ...
;                         const int h_ = it >> 4, y_ = it & 15, qb_ = ps ? 31 - y_ : y_;
;                         const float* kmp_h = W_kmp + h_ * 128;
;                         __syncthreads();
;                         for (int e = ftid; e < qb_ * 32; e += NWAVES * 64) { const int n = e >> 5, d4 = (e & 31) * 4;
;                             const f32x4 a = *(const f32x4*)(kmp_h + (size_t)n * D + d4), bq = *(const f32x4*)(kmp_h + (size_t)(32 + n) * D + d4);
;                             *(LAS f32x4*)(km + n * 136 + (d4 >> 6) * 68 + (d4 & 63)) = a + bq; }
;                         __syncthreads();
;                         const int row = ftid >> 1, half = ftid & 1;
;                         float q[64];
;                         { const bf16_t* qp = W_qb + ((size_t)h_ * T + qb_ * 256 + row) * 128 + half * 64;
; #pragma unroll
;                           for (int i = 0; i < 8; ++i) { const bf16x8 v = *(const bf16x8*)(qp + i * 8);
;     ...
;                             const float kmaxv = __uint_as_float(__hip_atomic_load(W_ctl + 12288 + j * 64 + h_, __ATOMIC_RELAXED, __HIP_MEMORY_SCOPE_AGENT));
.LBB0_565:
	s_and_b64 s[10:11], s[12:13], exec
	s_cselect_b32 s35, s31, s33
	s_lshl_b32 s64, s35, 8
	v_lshl_add_u64 v[124:125], v[6:7], 0, s[64:65]
	v_lshlrev_b64 v[124:125], 8, v[124:125]
	v_lshl_add_u64 v[124:125], v[2:3], 0, v[124:125]
	global_load_dword v137, v129, s[8:9] sc1
	global_load_dwordx4 v[92:95], v[124:125], off
	global_load_dwordx4 v[96:99], v[124:125], off offset:16
	global_load_dwordx4 v[100:103], v[124:125], off offset:32
	global_load_dwordx4 v[104:107], v[124:125], off offset:48
	global_load_dwordx4 v[108:111], v[124:125], off offset:64
	global_load_dwordx4 v[112:115], v[124:125], off offset:80
	global_load_dwordx4 v[116:119], v[124:125], off offset:96
	global_load_dwordx4 v[120:123], v[124:125], off offset:112
	s_lshl_b32 s16, s35, 5
	v_cmp_gt_i32_e32 vcc, s16, v74
	s_barrier
	s_and_saveexec_b64 s[10:11], vcc
	v_readlane_b32 s36, v252, 12
	s_cbranch_execz .LBB0_568
	s_mov_b64 s[14:15], 0
	v_mov_b32_e32 v8, v79
	v_mov_b32_e32 v9, v74

; __global__ void __launch_bounds__(NWAVES * 64, 2) mk_fwd(Args args) {
;     ...
;                         const int row = ftid >> 1, half = ftid & 1;
;                         float q[64];
;                         { const bf16_t* qp = W_qb + ((size_t)h_ * T + qb_ * 256 + row) * 128 + half * 64;
; #pragma unroll
;                           for (int i = 0; i < 8; ++i) { const bf16x8 v = *(const bf16x8*)(qp + i * 8);
; #pragma unroll
;                               for (int jj = 0; jj < 8; ++jj) q[i * 8 + jj] = bf2f((unsigned short)v[jj]); } }
;                         float v0 = -INFINITY, v1 = -INFINITY, v2 = -INFINITY; int i0 = -1, i1 = -1, i2 = -1;
.LBB0_568:
	s_or_b64 exec, exec, s[10:11]
	s_lshl_b32 s64, s35, 8
	v_lshl_add_u64 v[8:9], v[6:7], 0, s[64:65]
	s_waitcnt lgkmcnt(0)
	s_barrier
	s_xor_b64 s[10:11], s[12:13], -1
	s_waitcnt vmcnt(7)
	v_lshlrev_b32_e32 v10, 16, v92
	v_and_b32_e32 v11, 0xffff0000, v92
	v_lshlrev_b32_e32 v12, 16, v93
	v_and_b32_e32 v13, 0xffff0000, v93
	v_lshlrev_b32_e32 v14, 16, v94
	v_and_b32_e32 v15, 0xffff0000, v94
	v_lshlrev_b32_e32 v16, 16, v95
	v_and_b32_e32 v17, 0xffff0000, v95
	s_waitcnt vmcnt(6)
	v_lshlrev_b32_e32 v18, 16, v96
	v_and_b32_e32 v19, 0xffff0000, v96
	v_lshlrev_b32_e32 v20, 16, v97
	v_and_b32_e32 v21, 0xffff0000, v97
	v_lshlrev_b32_e32 v22, 16, v98
	v_and_b32_e32 v23, 0xffff0000, v98
	v_lshlrev_b32_e32 v24, 16, v99
	v_and_b32_e32 v25, 0xffff0000, v99
	s_waitcnt vmcnt(5)
	v_lshlrev_b32_e32 v26, 16, v100
	v_and_b32_e32 v27, 0xffff0000, v100
	v_lshlrev_b32_e32 v28, 16, v101
	v_and_b32_e32 v29, 0xffff0000, v101
	v_lshlrev_b32_e32 v30, 16, v102
	v_and_b32_e32 v31, 0xffff0000, v102
	v_lshlrev_b32_e32 v32, 16, v103
	v_and_b32_e32 v33, 0xffff0000, v103
	s_waitcnt vmcnt(4)
	v_lshlrev_b32_e32 v34, 16, v104
	v_and_b32_e32 v35, 0xffff0000, v104
	v_lshlrev_b32_e32 v36, 16, v105
	v_and_b32_e32 v37, 0xffff0000, v105
	v_lshlrev_b32_e32 v38, 16, v106
	v_and_b32_e32 v39, 0xffff0000, v106
	v_lshlrev_b32_e32 v40, 16, v107
	v_and_b32_e32 v41, 0xffff0000, v107
	s_waitcnt vmcnt(3)
	v_lshlrev_b32_e32 v42, 16, v108
	v_and_b32_e32 v43, 0xffff0000, v108
	v_lshlrev_b32_e32 v44, 16, v109
	v_and_b32_e32 v45, 0xffff0000, v109
	v_lshlrev_b32_e32 v46, 16, v110
	v_and_b32_e32 v47, 0xffff0000, v110
	v_lshlrev_b32_e32 v48, 16, v111
	v_and_b32_e32 v49, 0xffff0000, v111
	s_waitcnt vmcnt(2)
	v_lshlrev_b32_e32 v50, 16, v112
	v_and_b32_e32 v51, 0xffff0000, v112
	v_lshlrev_b32_e32 v52, 16, v113
	v_and_b32_e32 v53, 0xffff0000, v113
	v_lshlrev_b32_e32 v54, 16, v114
	v_and_b32_e32 v55, 0xffff0000, v114
	v_lshlrev_b32_e32 v56, 16, v115
	v_and_b32_e32 v57, 0xffff0000, v115
	s_waitcnt vmcnt(1)
	v_lshlrev_b32_e32 v58, 16, v116
	v_and_b32_e32 v59, 0xffff0000, v116
	v_lshlrev_b32_e32 v60, 16, v117
	v_and_b32_e32 v61, 0xffff0000, v117
	v_lshlrev_b32_e32 v62, 16, v118
	v_and_b32_e32 v63, 0xffff0000, v118
	v_lshlrev_b32_e32 v64, 16, v119
	v_and_b32_e32 v65, 0xffff0000, v119
	s_waitcnt vmcnt(0)
	v_lshlrev_b32_e32 v66, 16, v120
	v_and_b32_e32 v67, 0xffff0000, v120
	v_lshlrev_b32_e32 v68, 16, v121
	v_and_b32_e32 v69, 0xffff0000, v121
	v_lshlrev_b32_e32 v70, 16, v122
	v_and_b32_e32 v71, 0xffff0000, v122
	v_lshlrev_b32_e32 v72, 16, v123
	v_and_b32_e32 v73, 0xffff0000, v123
	v_mov_b32_e32 v85, -1
	v_mov_b32_e32 v84, -1
	v_mov_b32_e32 v83, -1
	v_mov_b32_e32 v124, 0xff800000
	v_mov_b32_e32 v125, 0xff800000
	v_mov_b32_e32 v126, 0xff800000
	v_add_u32_e32 v88, 0x10800, v80
	s_mov_b32 s36, 0
	s_mov_b32 s37, 0
	s_cmp_eq_u32 s35, 0
	s_cbranch_scc1 .Lpa_done

; __global__ void __launch_bounds__(NWAVES * 64, 2) mk_fwd(Args args) {
;     ...
;                         {
;                             float l1 = 0.f;
; #pragma unroll
;                             for (int i = 0; i < 64; ++i) l1 += fabsf(q[i]);
;                             l1 += __shfl_xor(l1, 1);
;                             const float kmaxv = __uint_as_float(__hip_atomic_load(W_ctl + 12288 + j * 64 + h_, __ATOMIC_RELAXED, __HIP_MEMORY_SCOPE_AGENT));
;                             const float Bq = mb::SCALE * l1 * kmaxv * 1.02f, slope = exp2f(-(float)(h_ + 1) * 0.5f);
;                             const float Dz = (2.f * Bq + 104.f) / slope, posf = (float)(qb_ * 256 + row - 255);
;                             if (i0 >= 0 && posf - (float)(i0 * 256) > Dz) i0 = -1;
;                             if (i1 >= 0 && posf - (float)(i1 * 256) > Dz) i1 = -1;
;                             if (i2 >= 0 && posf - (float)(i2 * 256) > Dz) i2 = -1;
.Lpa_done:
	v_add_f32_e64 v10, |v10|, |v11|
	v_add_f32_e64 v10, v10, |v12|
	v_add_f32_e64 v10, v10, |v13|
	v_add_f32_e64 v10, v10, |v14|
	v_add_f32_e64 v10, v10, |v15|
	v_add_f32_e64 v10, v10, |v16|
	v_add_f32_e64 v10, v10, |v17|
	v_add_f32_e64 v10, v10, |v18|
	v_add_f32_e64 v10, v10, |v19|
	v_add_f32_e64 v10, v10, |v20|
	v_add_f32_e64 v10, v10, |v21|
	v_add_f32_e64 v10, v10, |v22|
	v_add_f32_e64 v10, v10, |v23|
	v_add_f32_e64 v10, v10, |v24|
	v_add_f32_e64 v10, v10, |v25|
	v_add_f32_e64 v10, v10, |v26|
	v_add_f32_e64 v10, v10, |v27|
	v_add_f32_e64 v10, v10, |v28|
	v_add_f32_e64 v10, v10, |v29|
	v_add_f32_e64 v10, v10, |v30|
	v_add_f32_e64 v10, v10, |v31|
	v_add_f32_e64 v10, v10, |v32|
	v_add_f32_e64 v10, v10, |v33|
	v_add_f32_e64 v10, v10, |v34|
	v_add_f32_e64 v10, v10, |v35|
	v_add_f32_e64 v10, v10, |v36|
	v_add_f32_e64 v10, v10, |v37|
	v_add_f32_e64 v10, v10, |v38|
	v_add_f32_e64 v10, v10, |v39|
	v_add_f32_e64 v10, v10, |v40|
	v_add_f32_e64 v10, v10, |v41|
	v_add_f32_e64 v10, v10, |v42|
	v_add_f32_e64 v10, v10, |v43|
	v_add_f32_e64 v10, v10, |v44|
	v_add_f32_e64 v10, v10, |v45|
	v_add_f32_e64 v10, v10, |v46|
	v_add_f32_e64 v10, v10, |v47|
	v_add_f32_e64 v10, v10, |v48|
	v_add_f32_e64 v10, v10, |v49|
	v_add_f32_e64 v10, v10, |v50|
	v_add_f32_e64 v10, v10, |v51|
	v_add_f32_e64 v10, v10, |v52|
	v_add_f32_e64 v10, v10, |v53|
	v_add_f32_e64 v10, v10, |v54|
	v_add_f32_e64 v10, v10, |v55|
	v_add_f32_e64 v10, v10, |v56|
	v_add_f32_e64 v10, v10, |v57|
	v_add_f32_e64 v10, v10, |v58|
	v_add_f32_e64 v10, v10, |v59|
	v_add_f32_e64 v10, v10, |v60|
	v_add_f32_e64 v10, v10, |v61|
	v_add_f32_e64 v10, v10, |v62|
	v_add_f32_e64 v10, v10, |v63|
	v_add_f32_e64 v10, v10, |v64|
	v_add_f32_e64 v10, v10, |v65|
	v_add_f32_e64 v10, v10, |v66|
	v_add_f32_e64 v10, v10, |v67|
	v_add_f32_e64 v10, v10, |v68|
	v_add_f32_e64 v10, v10, |v69|
	v_add_f32_e64 v10, v10, |v70|
	v_add_f32_e64 v10, v10, |v71|
	v_add_f32_e64 v10, v10, |v72|
	v_add_f32_e64 v10, v10, |v73|
	ds_bpermute_b32 v11, v76, v10
	s_waitcnt lgkmcnt(0)
	v_add_f32_e32 v10, v10, v11
	v_mul_f32_e32 v10, 0x3db504f3, v10
	s_waitcnt vmcnt(0)
	v_mul_f32_e32 v10, v10, v137
	v_mul_f32_e32 v10, 0x3f828f5c, v10
	v_fmaak_f32 v10, 2.0, v10, 0x42d00000
	v_div_scale_f32 v11, s[12:13], v82, v82, v10
	v_rcp_f32_e32 v12, v11
	s_nop 0
	v_fma_f32 v13, -v11, v12, 1.0
	v_fmac_f32_e32 v12, v13, v12
	v_div_scale_f32 v13, vcc, v10, v82, v10
	v_mul_f32_e32 v14, v13, v12
	v_fma_f32 v15, -v11, v14, v13
	v_fmac_f32_e32 v14, v15, v12
	v_fma_f32 v11, -v11, v14, v13
	v_div_fmas_f32 v11, v11, v12, v14
	v_div_fixup_f32 v10, v11, v82, v10
	v_add_u32_e32 v11, s64, v77
	v_cvt_f32_i32_e32 v11, v11
	v_cmp_lt_i32_e32 vcc, -1, v85
	s_and_saveexec_b64 s[12:13], vcc
	s_cbranch_execz .LBB0_587
	v_lshlrev_b32_e32 v12, 8, v85
	v_cvt_f32_u32_e32 v12, v12
	v_sub_f32_e32 v12, v11, v12
	v_cmp_gt_f32_e32 vcc, v12, v10
	s_and_saveexec_b64 s[14:15], vcc
	v_mov_b32_e32 v85, -1
	s_or_b64 exec, exec, s[14:15]
	s_or_b64 exec, exec, s[12:13]
	v_cmp_lt_i32_e32 vcc, -1, v84
	s_and_saveexec_b64 s[12:13], vcc
	s_cbranch_execnz .LBB0_588
